# early-start gather, ids loaded first, e2f after gather (4 partial sums), finalize kernargs hoisted
# baseline (speedup 1.0000x reference)
_Z7vq_mainPKfPKiS0_PfPhPdPi:
	s_load_dwordx4 s[4:7], s[0:1], 0x0
	s_load_dwordx2 s[22:23], s[0:1], 0x10
	s_load_dwordx2 s[20:21], s[0:1], 0x18
	s_load_dwordx4 s[12:15], s[0:1], 0x20
	s_load_dwordx2 s[10:11], s[0:1], 0x30
	s_and_b32 s3, s2, 7
	s_lshl_b32 s3, s3, 6
	s_lshr_b32 s16, s2, 3
	s_add_i32 s16, s16, s3
	s_lshr_b32 s18, s16, 5
	s_mov_b32 s19, 0
	s_and_b32 s28, s16, 31
	s_lshl_b32 s28, s28, 4
	s_add_i32 s29, s28, 1
	v_readfirstlane_b32 s17, v0
	v_and_b32_e32 v1, 63, v0
	v_lshlrev_b32_e32 v224, 4, v0
	s_lshr_b32 s17, s17, 6
	s_lshl_b32 s24, s17, 4
	s_lshl_b32 s30, s18, 15
	s_lshl_b32 s31, s18, 23
	v_add_u32_e32 v225, 0x1000, v224
	v_add_u32_e32 v226, 0x2000, v224
	v_add_u32_e32 v227, 0x3000, v224
	v_add_u32_e32 v228, 0x4000, v224
	v_add_u32_e32 v229, 0x5000, v224
	v_add_u32_e32 v230, 0x6000, v224
	v_add_u32_e32 v231, 0x7000, v224
	s_waitcnt lgkmcnt(0)
	s_add_u32 s34, s6, s30
	s_addc_u32 s35, s7, 0
	s_add_u32 s32, s4, s31
	s_addc_u32 s33, s5, 0
	global_load_dwordx4 v[130:133], v224, s[34:35]
	global_load_dwordx4 v[134:137], v225, s[34:35]
	global_load_dwordx4 v[138:141], v226, s[34:35]
	global_load_dwordx4 v[142:145], v227, s[34:35]
	global_load_dwordx4 v[146:149], v228, s[34:35]
	global_load_dwordx4 v[150:153], v229, s[34:35]
	global_load_dwordx4 v[154:157], v230, s[34:35]
	global_load_dwordx4 v[158:161], v231, s[34:35]
	v_and_b32_e32 v198, 15, v0
	v_or_b32_e32 v198, s24, v198
	v_and_b32_e32 v199, 48, v0
	v_lshl_or_b32 v198, v198, 10, v199
	global_load_dwordx4 v[62:65], v198, s[22:23] offset:0
	global_load_dwordx4 v[58:61], v198, s[22:23] offset:64
	global_load_dwordx4 v[54:57], v198, s[22:23] offset:128
	global_load_dwordx4 v[50:53], v198, s[22:23] offset:192
	global_load_dwordx4 v[46:49], v198, s[22:23] offset:256
	global_load_dwordx4 v[42:45], v198, s[22:23] offset:320
	global_load_dwordx4 v[38:41], v198, s[22:23] offset:384
	global_load_dwordx4 v[34:37], v198, s[22:23] offset:448
	global_load_dwordx4 v[30:33], v198, s[22:23] offset:512
	global_load_dwordx4 v[26:29], v198, s[22:23] offset:576
	global_load_dwordx4 v[22:25], v198, s[22:23] offset:640
	global_load_dwordx4 v[18:21], v198, s[22:23] offset:704
	global_load_dwordx4 v[14:17], v198, s[22:23] offset:768
	global_load_dwordx4 v[10:13], v198, s[22:23] offset:832
	global_load_dwordx4 v[6:9], v198, s[22:23] offset:896
	global_load_dwordx4 v[2:5], v198, s[22:23] offset:960
	v_mov_b32_e32 v194, 1
	v_mov_b32_e32 v195, 4
	v_mov_b32_e32 v196, 0x11100
	v_lshlrev_b32_e32 v197, 8, v0
	v_lshlrev_b32_e32 v222, 3, v0
	v_lshlrev_b32_e32 v218, 4, v1
	v_lshlrev_b32_e32 v219, 3, v1
	v_mov_b32_e32 v234, 0
	v_mov_b32_e32 v235, 0
	v_mov_b32_e32 v232, 0
	ds_write_b64 v222, v[234:235] offset:32768
	ds_write_b64 v222, v[234:235] offset:34832
	ds_write_b64 v222, v[234:235] offset:36896
	ds_write_b64 v222, v[234:235] offset:38960
	ds_write_b64 v222, v[234:235] offset:41024
	ds_write_b64 v222, v[234:235] offset:43088
	ds_write_b64 v222, v[234:235] offset:45152
	ds_write_b64 v222, v[234:235] offset:47216
	ds_write_b64 v222, v[234:235] offset:49280
	ds_write_b64 v222, v[234:235] offset:51344
	ds_write_b64 v222, v[234:235] offset:53408
	ds_write_b64 v222, v[234:235] offset:55472
	ds_write_b64 v222, v[234:235] offset:57536
	ds_write_b64 v222, v[234:235] offset:59600
	ds_write_b64 v222, v[234:235] offset:61664
	ds_write_b64 v222, v[234:235] offset:63728
	v_cmp_gt_u32_e32 vcc, 16, v0
	s_and_saveexec_b64 s[30:31], vcc
	v_lshl_add_u32 v228, v0, 2, v196
	ds_write_b32 v228, v234
	ds_write_b32 v228, v234 offset:1024
	s_mov_b64 exec, s[30:31]
	s_lshl_b32 s84, s17, 8
	s_mov_b32 s9, 0
	s_waitcnt lgkmcnt(0)
	s_barrier
	s_waitcnt vmcnt(16)
	v_subrev_u32_e32 v130, s29, v130
	v_subrev_u32_e32 v131, s29, v131
	v_subrev_u32_e32 v132, s29, v132
	v_subrev_u32_e32 v133, s29, v133
	v_cmp_gt_u32_e64 s[36:37], 16, v130
	v_cmp_gt_u32_e64 s[38:39], 16, v131
	v_cmp_gt_u32_e64 s[40:41], 16, v132
	v_cmp_gt_u32_e64 s[42:43], 16, v133
	s_andn2_b64 s[88:89], s[38:39], s[36:37]
	s_or_b64 s[94:95], s[36:37], s[38:39]
	s_andn2_b64 s[90:91], s[40:41], s[94:95]
	s_or_b64 s[94:95], s[94:95], s[40:41]
	s_andn2_b64 s[92:93], s[42:43], s[94:95]
	s_or_b64 s[96:97], s[94:95], s[42:43]
	s_mov_b64 s[98:99], s[96:97]
	v_add_u32_e32 v223, 48, v133
	v_add_u32_e32 v229, 32, v132
	v_cndmask_b32_e64 v223, v223, v229, s[90:91]
	v_add_u32_e32 v229, 16, v131
	v_cndmask_b32_e64 v223, v223, v229, s[88:89]
	v_cndmask_b32_e64 v223, v223, v130, s[36:37]
	s_cmp_eq_u64 s[96:97], 0
	s_cbranch_scc1 .Le_done
	s_ff1_i32_b64 s80, s[96:97]
	s_bitset0_b64 s[96:97], s80
	v_readlane_b32 s81, v223, s80
	s_and_b32 s82, s81, 15
	v_writelane_b32 v232, s82, 0
	s_lshr_b32 s81, s81, 4
	s_lshl_b32 s83, s80, 2
	s_add_u32 s81, s81, s83
	s_add_u32 s81, s81, s84
	s_lshl_b32 s81, s81, 10
	s_add_u32 s86, s32, s81
	s_addc_u32 s87, s33, 0
	global_load_dwordx4 v[66:69], v218, s[86:87] nt
	s_mov_b32 s9, 1
	s_cmp_eq_u64 s[96:97], 0
	s_cbranch_scc1 .Le_done
	s_ff1_i32_b64 s80, s[96:97]
	s_bitset0_b64 s[96:97], s80
	v_readlane_b32 s81, v223, s80
	s_and_b32 s82, s81, 15
	v_writelane_b32 v232, s82, 1
	s_lshr_b32 s81, s81, 4
	s_lshl_b32 s83, s80, 2
	s_add_u32 s81, s81, s83
	s_add_u32 s81, s81, s84
	s_lshl_b32 s81, s81, 10
	s_add_u32 s86, s32, s81
	s_addc_u32 s87, s33, 0
	global_load_dwordx4 v[70:73], v218, s[86:87] nt
	s_mov_b32 s9, 2
	s_cmp_eq_u64 s[96:97], 0
	s_cbranch_scc1 .Le_done
	s_ff1_i32_b64 s80, s[96:97]
	s_bitset0_b64 s[96:97], s80
	v_readlane_b32 s81, v223, s80
	s_and_b32 s82, s81, 15
	v_writelane_b32 v232, s82, 2
	s_lshr_b32 s81, s81, 4
	s_lshl_b32 s83, s80, 2
	s_add_u32 s81, s81, s83
	s_add_u32 s81, s81, s84
	s_lshl_b32 s81, s81, 10
	s_add_u32 s86, s32, s81
	s_addc_u32 s87, s33, 0
	global_load_dwordx4 v[74:77], v218, s[86:87] nt
	s_mov_b32 s9, 3
	s_cmp_eq_u64 s[96:97], 0
	s_cbranch_scc1 .Le_done
	s_ff1_i32_b64 s80, s[96:97]
	s_bitset0_b64 s[96:97], s80
	v_readlane_b32 s81, v223, s80
	s_and_b32 s82, s81, 15
	v_writelane_b32 v232, s82, 3
	s_lshr_b32 s81, s81, 4
	s_lshl_b32 s83, s80, 2
	s_add_u32 s81, s81, s83
	s_add_u32 s81, s81, s84
	s_lshl_b32 s81, s81, 10
	s_add_u32 s86, s32, s81
	s_addc_u32 s87, s33, 0
	global_load_dwordx4 v[78:81], v218, s[86:87] nt
	s_mov_b32 s9, 4
	s_cmp_eq_u64 s[96:97], 0
	s_cbranch_scc1 .Le_done
	s_ff1_i32_b64 s80, s[96:97]
	s_bitset0_b64 s[96:97], s80
	v_readlane_b32 s81, v223, s80
	s_and_b32 s82, s81, 15
	v_writelane_b32 v232, s82, 4
	s_lshr_b32 s81, s81, 4
	s_lshl_b32 s83, s80, 2
	s_add_u32 s81, s81, s83
	s_add_u32 s81, s81, s84
	s_lshl_b32 s81, s81, 10
	s_add_u32 s86, s32, s81
	s_addc_u32 s87, s33, 0
	global_load_dwordx4 v[82:85], v218, s[86:87] nt
	s_mov_b32 s9, 5
	s_cmp_eq_u64 s[96:97], 0
	s_cbranch_scc1 .Le_done
	s_ff1_i32_b64 s80, s[96:97]
	s_bitset0_b64 s[96:97], s80
	v_readlane_b32 s81, v223, s80
	s_and_b32 s82, s81, 15
	v_writelane_b32 v232, s82, 5
	s_lshr_b32 s81, s81, 4
	s_lshl_b32 s83, s80, 2
	s_add_u32 s81, s81, s83
	s_add_u32 s81, s81, s84
	s_lshl_b32 s81, s81, 10
	s_add_u32 s86, s32, s81
	s_addc_u32 s87, s33, 0
	global_load_dwordx4 v[86:89], v218, s[86:87] nt
	s_mov_b32 s9, 6
	s_cmp_eq_u64 s[96:97], 0
	s_cbranch_scc1 .Le_done
	s_ff1_i32_b64 s80, s[96:97]
	s_bitset0_b64 s[96:97], s80
	v_readlane_b32 s81, v223, s80
	s_and_b32 s82, s81, 15
	v_writelane_b32 v232, s82, 6
	s_lshr_b32 s81, s81, 4
	s_lshl_b32 s83, s80, 2
	s_add_u32 s81, s81, s83
	s_add_u32 s81, s81, s84
	s_lshl_b32 s81, s81, 10
	s_add_u32 s86, s32, s81
	s_addc_u32 s87, s33, 0
	global_load_dwordx4 v[90:93], v218, s[86:87] nt
	s_mov_b32 s9, 7
	s_cmp_eq_u64 s[96:97], 0
	s_cbranch_scc1 .Le_done
	s_ff1_i32_b64 s80, s[96:97]
	s_bitset0_b64 s[96:97], s80
	v_readlane_b32 s81, v223, s80
	s_and_b32 s82, s81, 15
	v_writelane_b32 v232, s82, 7
	s_lshr_b32 s81, s81, 4
	s_lshl_b32 s83, s80, 2
	s_add_u32 s81, s81, s83
	s_add_u32 s81, s81, s84
	s_lshl_b32 s81, s81, 10
	s_add_u32 s86, s32, s81
	s_addc_u32 s87, s33, 0
	global_load_dwordx4 v[94:97], v218, s[86:87] nt
	s_mov_b32 s9, 8
	s_cmp_eq_u64 s[96:97], 0
	s_cbranch_scc1 .Le_done
	s_ff1_i32_b64 s80, s[96:97]
	s_bitset0_b64 s[96:97], s80
	v_readlane_b32 s81, v223, s80
	s_and_b32 s82, s81, 15
	v_writelane_b32 v232, s82, 8
	s_lshr_b32 s81, s81, 4
	s_lshl_b32 s83, s80, 2
	s_add_u32 s81, s81, s83
	s_add_u32 s81, s81, s84
	s_lshl_b32 s81, s81, 10
	s_add_u32 s86, s32, s81
	s_addc_u32 s87, s33, 0
	global_load_dwordx4 v[98:101], v218, s[86:87] nt
	s_mov_b32 s9, 9
	s_cmp_eq_u64 s[96:97], 0
	s_cbranch_scc1 .Le_done
	s_ff1_i32_b64 s80, s[96:97]
	s_bitset0_b64 s[96:97], s80
	v_readlane_b32 s81, v223, s80
	s_and_b32 s82, s81, 15
	v_writelane_b32 v232, s82, 9
	s_lshr_b32 s81, s81, 4
	s_lshl_b32 s83, s80, 2
	s_add_u32 s81, s81, s83
	s_add_u32 s81, s81, s84
	s_lshl_b32 s81, s81, 10
	s_add_u32 s86, s32, s81
	s_addc_u32 s87, s33, 0
	global_load_dwordx4 v[102:105], v218, s[86:87] nt
	s_mov_b32 s9, 10
	s_cmp_eq_u64 s[96:97], 0
	s_cbranch_scc1 .Le_done
	s_ff1_i32_b64 s80, s[96:97]
	s_bitset0_b64 s[96:97], s80
	v_readlane_b32 s81, v223, s80
	s_and_b32 s82, s81, 15
	v_writelane_b32 v232, s82, 10
	s_lshr_b32 s81, s81, 4
	s_lshl_b32 s83, s80, 2
	s_add_u32 s81, s81, s83
	s_add_u32 s81, s81, s84
	s_lshl_b32 s81, s81, 10
	s_add_u32 s86, s32, s81
	s_addc_u32 s87, s33, 0
	global_load_dwordx4 v[106:109], v218, s[86:87] nt
	s_mov_b32 s9, 11
	s_cmp_eq_u64 s[96:97], 0
	s_cbranch_scc1 .Le_done
	s_ff1_i32_b64 s80, s[96:97]
	s_bitset0_b64 s[96:97], s80
	v_readlane_b32 s81, v223, s80
	s_and_b32 s82, s81, 15
	v_writelane_b32 v232, s82, 11
	s_lshr_b32 s81, s81, 4
	s_lshl_b32 s83, s80, 2
	s_add_u32 s81, s81, s83
	s_add_u32 s81, s81, s84
	s_lshl_b32 s81, s81, 10
	s_add_u32 s86, s32, s81
	s_addc_u32 s87, s33, 0
	global_load_dwordx4 v[110:113], v218, s[86:87] nt
	s_mov_b32 s9, 12
	s_cmp_eq_u64 s[96:97], 0
	s_cbranch_scc1 .Le_done
	s_ff1_i32_b64 s80, s[96:97]
	s_bitset0_b64 s[96:97], s80
	v_readlane_b32 s81, v223, s80
	s_and_b32 s82, s81, 15
	v_writelane_b32 v232, s82, 12
	s_lshr_b32 s81, s81, 4
	s_lshl_b32 s83, s80, 2
	s_add_u32 s81, s81, s83
	s_add_u32 s81, s81, s84
	s_lshl_b32 s81, s81, 10
	s_add_u32 s86, s32, s81
	s_addc_u32 s87, s33, 0
	global_load_dwordx4 v[114:117], v218, s[86:87] nt
	s_mov_b32 s9, 13
	s_cmp_eq_u64 s[96:97], 0
	s_cbranch_scc1 .Le_done
	s_ff1_i32_b64 s80, s[96:97]
	s_bitset0_b64 s[96:97], s80
	v_readlane_b32 s81, v223, s80
	s_and_b32 s82, s81, 15
	v_writelane_b32 v232, s82, 13
	s_lshr_b32 s81, s81, 4
	s_lshl_b32 s83, s80, 2
	s_add_u32 s81, s81, s83
	s_add_u32 s81, s81, s84
	s_lshl_b32 s81, s81, 10
	s_add_u32 s86, s32, s81
	s_addc_u32 s87, s33, 0
	global_load_dwordx4 v[118:121], v218, s[86:87] nt
	s_mov_b32 s9, 14
	s_cmp_eq_u64 s[96:97], 0
	s_cbranch_scc1 .Le_done
	s_ff1_i32_b64 s80, s[96:97]
	s_bitset0_b64 s[96:97], s80
	v_readlane_b32 s81, v223, s80
	s_and_b32 s82, s81, 15
	v_writelane_b32 v232, s82, 14
	s_lshr_b32 s81, s81, 4
	s_lshl_b32 s83, s80, 2
	s_add_u32 s81, s81, s83
	s_add_u32 s81, s81, s84
	s_lshl_b32 s81, s81, 10
	s_add_u32 s86, s32, s81
	s_addc_u32 s87, s33, 0
	global_load_dwordx4 v[122:125], v218, s[86:87] nt
	s_mov_b32 s9, 15
	s_cmp_eq_u64 s[96:97], 0
	s_cbranch_scc1 .Le_done
	s_ff1_i32_b64 s80, s[96:97]
	s_bitset0_b64 s[96:97], s80
	v_readlane_b32 s81, v223, s80
	s_and_b32 s82, s81, 15
	v_writelane_b32 v232, s82, 15
	s_lshr_b32 s81, s81, 4
	s_lshl_b32 s83, s80, 2
	s_add_u32 s81, s81, s83
	s_add_u32 s81, s81, s84
	s_lshl_b32 s81, s81, 10
	s_add_u32 s86, s32, s81
	s_addc_u32 s87, s33, 0
	global_load_dwordx4 v[126:129], v218, s[86:87] nt
	s_mov_b32 s9, 16
.Le_done:
	s_andn2_b64 s[98:99], s[98:99], s[96:97]
	s_and_b64 s[94:95], s[36:37], s[98:99]
	s_andn2_b64 s[36:37], s[36:37], s[94:95]
	s_and_b64 s[94:95], s[88:89], s[98:99]
	s_andn2_b64 s[38:39], s[38:39], s[94:95]
	s_and_b64 s[94:95], s[90:91], s[98:99]
	s_andn2_b64 s[40:41], s[40:41], s[94:95]
	s_and_b64 s[94:95], s[92:93], s[98:99]
	s_andn2_b64 s[42:43], s[42:43], s[94:95]
	s_mov_b64 exec, s[98:99]
	v_and_b32_e32 v229, 15, v223
	v_lshl_add_u32 v229, v229, 2, v196
	ds_add_u32 v229, v194 offset:1024
	s_mov_b64 exec, -1
	v_subrev_u32_e32 v134, s29, v134
	v_subrev_u32_e32 v135, s29, v135
	v_subrev_u32_e32 v136, s29, v136
	v_subrev_u32_e32 v137, s29, v137
	v_subrev_u32_e32 v138, s29, v138
	v_subrev_u32_e32 v139, s29, v139
	v_subrev_u32_e32 v140, s29, v140
	v_subrev_u32_e32 v141, s29, v141
	v_subrev_u32_e32 v142, s29, v142
	v_subrev_u32_e32 v143, s29, v143
	v_subrev_u32_e32 v144, s29, v144
	v_subrev_u32_e32 v145, s29, v145
	v_subrev_u32_e32 v146, s29, v146
	v_subrev_u32_e32 v147, s29, v147
	v_subrev_u32_e32 v148, s29, v148
	v_subrev_u32_e32 v149, s29, v149
	v_subrev_u32_e32 v150, s29, v150
	v_subrev_u32_e32 v151, s29, v151
	v_subrev_u32_e32 v152, s29, v152
	v_subrev_u32_e32 v153, s29, v153
	v_subrev_u32_e32 v154, s29, v154
	v_subrev_u32_e32 v155, s29, v155
	v_subrev_u32_e32 v156, s29, v156
	v_subrev_u32_e32 v157, s29, v157
	v_subrev_u32_e32 v158, s29, v158
	v_subrev_u32_e32 v159, s29, v159
	v_subrev_u32_e32 v160, s29, v160
	v_subrev_u32_e32 v161, s29, v161
	v_cmp_gt_u32_e64 s[44:45], 16, v134
	v_cmp_gt_u32_e64 s[46:47], 16, v135
	v_cmp_gt_u32_e64 s[48:49], 16, v136
	v_cmp_gt_u32_e64 s[50:51], 16, v137
	v_cmp_gt_u32_e64 s[52:53], 16, v138
	v_cmp_gt_u32_e64 s[54:55], 16, v139
	v_cmp_gt_u32_e64 s[56:57], 16, v140
	v_cmp_gt_u32_e64 s[58:59], 16, v141
	v_cmp_gt_u32_e64 s[60:61], 16, v142
	v_cmp_gt_u32_e64 s[62:63], 16, v143
	v_cmp_gt_u32_e64 s[64:65], 16, v144
	v_cmp_gt_u32_e64 s[66:67], 16, v145
	v_cmp_gt_u32_e64 s[68:69], 16, v146
	v_cmp_gt_u32_e64 s[70:71], 16, v147
	v_cmp_gt_u32_e64 s[72:73], 16, v148
	v_cmp_gt_u32_e64 s[74:75], 16, v149
	v_cmp_gt_u32_e64 s[76:77], 16, v150
	v_cmp_gt_u32_e64 s[78:79], 16, v151
	v_cmp_gt_u32_e64 s[80:81], 16, v152
	v_cmp_gt_u32_e64 s[82:83], 16, v153
	v_cmp_gt_u32_e64 s[84:85], 16, v154
	v_cmp_gt_u32_e64 s[86:87], 16, v155
	v_cmp_gt_u32_e64 s[88:89], 16, v156
	v_cmp_gt_u32_e64 s[90:91], 16, v157
	v_cmp_gt_u32_e64 s[92:93], 16, v158
	v_cmp_gt_u32_e64 s[94:95], 16, v159
	v_cmp_gt_u32_e64 s[96:97], 16, v160
	v_cmp_gt_u32_e64 s[98:99], 16, v161
	s_mov_b64 exec, s[36:37]
	v_lshl_add_u32 v130, v130, 2, v196
	ds_add_u32 v130, v194
	s_mov_b64 exec, s[38:39]
	v_lshl_add_u32 v131, v131, 2, v196
	ds_add_u32 v131, v194
	s_mov_b64 exec, s[40:41]
	v_lshl_add_u32 v132, v132, 2, v196
	ds_add_u32 v132, v194
	s_mov_b64 exec, s[42:43]
	v_lshl_add_u32 v133, v133, 2, v196
	ds_add_u32 v133, v194
	s_mov_b64 exec, s[44:45]
	v_lshl_add_u32 v134, v134, 2, v196
	ds_add_u32 v134, v194
	s_mov_b64 exec, s[46:47]
	v_lshl_add_u32 v135, v135, 2, v196
	ds_add_u32 v135, v194
	s_mov_b64 exec, s[48:49]
	v_lshl_add_u32 v136, v136, 2, v196
	ds_add_u32 v136, v194
	s_mov_b64 exec, s[50:51]
	v_lshl_add_u32 v137, v137, 2, v196
	ds_add_u32 v137, v194
	s_mov_b64 exec, s[52:53]
	v_lshl_add_u32 v138, v138, 2, v196
	ds_add_u32 v138, v194
	s_mov_b64 exec, s[54:55]
	v_lshl_add_u32 v139, v139, 2, v196
	ds_add_u32 v139, v194
	s_mov_b64 exec, s[56:57]
	v_lshl_add_u32 v140, v140, 2, v196
	ds_add_u32 v140, v194
	s_mov_b64 exec, s[58:59]
	v_lshl_add_u32 v141, v141, 2, v196
	ds_add_u32 v141, v194
	s_mov_b64 exec, s[60:61]
	v_lshl_add_u32 v142, v142, 2, v196
	ds_add_u32 v142, v194
	s_mov_b64 exec, s[62:63]
	v_lshl_add_u32 v143, v143, 2, v196
	ds_add_u32 v143, v194
	s_mov_b64 exec, s[64:65]
	v_lshl_add_u32 v144, v144, 2, v196
	ds_add_u32 v144, v194
	s_mov_b64 exec, s[66:67]
	v_lshl_add_u32 v145, v145, 2, v196
	ds_add_u32 v145, v194
	s_mov_b64 exec, s[68:69]
	v_lshl_add_u32 v146, v146, 2, v196
	ds_add_u32 v146, v194
	s_mov_b64 exec, s[70:71]
	v_lshl_add_u32 v147, v147, 2, v196
	ds_add_u32 v147, v194
	s_mov_b64 exec, s[72:73]
	v_lshl_add_u32 v148, v148, 2, v196
	ds_add_u32 v148, v194
	s_mov_b64 exec, s[74:75]
	v_lshl_add_u32 v149, v149, 2, v196
	ds_add_u32 v149, v194
	s_mov_b64 exec, s[76:77]
	v_lshl_add_u32 v150, v150, 2, v196
	ds_add_u32 v150, v194
	s_mov_b64 exec, s[78:79]
	v_lshl_add_u32 v151, v151, 2, v196
	ds_add_u32 v151, v194
	s_mov_b64 exec, s[80:81]
	v_lshl_add_u32 v152, v152, 2, v196
	ds_add_u32 v152, v194
	s_mov_b64 exec, s[82:83]
	v_lshl_add_u32 v153, v153, 2, v196
	ds_add_u32 v153, v194
	s_mov_b64 exec, s[84:85]
	v_lshl_add_u32 v154, v154, 2, v196
	ds_add_u32 v154, v194
	s_mov_b64 exec, s[86:87]
	v_lshl_add_u32 v155, v155, 2, v196
	ds_add_u32 v155, v194
	s_mov_b64 exec, s[88:89]
	v_lshl_add_u32 v156, v156, 2, v196
	ds_add_u32 v156, v194
	s_mov_b64 exec, s[90:91]
	v_lshl_add_u32 v157, v157, 2, v196
	ds_add_u32 v157, v194
	s_mov_b64 exec, s[92:93]
	v_lshl_add_u32 v158, v158, 2, v196
	ds_add_u32 v158, v194
	s_mov_b64 exec, s[94:95]
	v_lshl_add_u32 v159, v159, 2, v196
	ds_add_u32 v159, v194
	s_mov_b64 exec, s[96:97]
	v_lshl_add_u32 v160, v160, 2, v196
	ds_add_u32 v160, v194
	s_mov_b64 exec, s[98:99]
	v_lshl_add_u32 v161, v161, 2, v196
	ds_add_u32 v161, v194
	s_mov_b64 exec, -1
	s_waitcnt lgkmcnt(0)
	s_barrier
	v_and_b32_e32 v228, 15, v0
	v_lshl_add_u32 v228, v228, 2, v196
	ds_read_b32 v229, v228
	s_waitcnt lgkmcnt(0)
	v_mov_b32_e32 v230, v229
	s_nop 1
	v_add_u32_dpp v230, v230, v230 row_shr:1 row_mask:0xf bank_mask:0xf bound_ctrl:1
	s_nop 1
	v_add_u32_dpp v230, v230, v230 row_shr:2 row_mask:0xf bank_mask:0xf bound_ctrl:1
	s_nop 1
	v_add_u32_dpp v230, v230, v230 row_shr:4 row_mask:0xf bank_mask:0xf bound_ctrl:1
	s_nop 1
	v_add_u32_dpp v230, v230, v230 row_shr:8 row_mask:0xf bank_mask:0xf bound_ctrl:1
	s_nop 1
	v_sub_u32_e32 v231, v230, v229
	v_lshlrev_b32_e32 v231, 2, v231
	v_readlane_b32 s8, v230, 15
	v_cmp_gt_u32_e32 vcc, 16, v1
	s_and_saveexec_b64 s[30:31], vcc
	s_cmp_lg_u32 s17, 0
	s_cbranch_scc1 .Lfront_nocursor
	ds_write_b32 v228, v231 offset:64

.Lg_alldone:
	s_waitcnt vmcnt(0)
	v_mul_f32_e32 v224, v62, v62
	v_mul_f32_e32 v225, v63, v63
	v_mul_f32_e32 v226, v64, v64
	v_mul_f32_e32 v227, v65, v65
	v_fmac_f32_e32 v224, v58, v58
	v_fmac_f32_e32 v225, v59, v59
	v_fmac_f32_e32 v226, v60, v60
	v_fmac_f32_e32 v227, v61, v61
	v_fmac_f32_e32 v224, v54, v54
	v_fmac_f32_e32 v225, v55, v55
	v_fmac_f32_e32 v226, v56, v56
	v_fmac_f32_e32 v227, v57, v57
	v_fmac_f32_e32 v224, v50, v50
	v_fmac_f32_e32 v225, v51, v51
	v_fmac_f32_e32 v226, v52, v52
	v_fmac_f32_e32 v227, v53, v53
	v_fmac_f32_e32 v224, v46, v46
	v_fmac_f32_e32 v225, v47, v47
	v_fmac_f32_e32 v226, v48, v48
	v_fmac_f32_e32 v227, v49, v49
	v_fmac_f32_e32 v224, v42, v42
	v_fmac_f32_e32 v225, v43, v43
	v_fmac_f32_e32 v226, v44, v44
	v_fmac_f32_e32 v227, v45, v45
	v_fmac_f32_e32 v224, v38, v38
	v_fmac_f32_e32 v225, v39, v39
	v_fmac_f32_e32 v226, v40, v40
	v_fmac_f32_e32 v227, v41, v41
	v_fmac_f32_e32 v224, v34, v34
	v_fmac_f32_e32 v225, v35, v35
	v_fmac_f32_e32 v226, v36, v36
	v_fmac_f32_e32 v227, v37, v37
	v_fmac_f32_e32 v224, v30, v30
	v_fmac_f32_e32 v225, v31, v31
	v_fmac_f32_e32 v226, v32, v32
	v_fmac_f32_e32 v227, v33, v33
	v_fmac_f32_e32 v224, v26, v26
	v_fmac_f32_e32 v225, v27, v27
	v_fmac_f32_e32 v226, v28, v28
	v_fmac_f32_e32 v227, v29, v29
	v_fmac_f32_e32 v224, v22, v22
	v_fmac_f32_e32 v225, v23, v23
	v_fmac_f32_e32 v226, v24, v24
	v_fmac_f32_e32 v227, v25, v25
	v_fmac_f32_e32 v224, v18, v18
	v_fmac_f32_e32 v225, v19, v19
	v_fmac_f32_e32 v226, v20, v20
	v_fmac_f32_e32 v227, v21, v21
	v_fmac_f32_e32 v224, v14, v14
	v_fmac_f32_e32 v225, v15, v15
	v_fmac_f32_e32 v226, v16, v16
	v_fmac_f32_e32 v227, v17, v17
	v_fmac_f32_e32 v224, v10, v10
	v_fmac_f32_e32 v225, v11, v11
	v_fmac_f32_e32 v226, v12, v12
	v_fmac_f32_e32 v227, v13, v13
	v_fmac_f32_e32 v224, v6, v6
	v_fmac_f32_e32 v225, v7, v7
	v_fmac_f32_e32 v226, v8, v8
	v_fmac_f32_e32 v227, v9, v9
	v_fmac_f32_e32 v224, v2, v2
	v_fmac_f32_e32 v225, v3, v3
	v_fmac_f32_e32 v226, v4, v4
	v_fmac_f32_e32 v227, v5, v5
	v_add_f32_e32 v224, v224, v225
	v_add_f32_e32 v226, v226, v227
	v_add_f32_e32 v224, v224, v226
	v_mbcnt_lo_u32_b32 v225, -1, 0
	v_mbcnt_hi_u32_b32 v225, -1, v225
	v_xor_b32_e32 v226, 16, v225
	v_lshlrev_b32_e32 v226, 2, v226
	ds_bpermute_b32 v226, v226, v224
	v_xor_b32_e32 v227, 32, v225
	v_lshlrev_b32_e32 v227, 2, v227
	s_waitcnt lgkmcnt(0)
	v_add_f32_e32 v224, v224, v226
	ds_bpermute_b32 v227, v227, v224
	v_add_u32_e32 v226, s24, v1
	v_lshlrev_b32_e32 v226, 2, v226
	v_add_u32_e32 v226, 0x11300, v226
	v_cmp_gt_u32_e32 vcc, 16, v1
	s_and_saveexec_b64 s[30:31], vcc
	s_waitcnt lgkmcnt(0)
	v_add_f32_e32 v224, v224, v227
	ds_write_b32 v226, v224
	s_mov_b64 exec, s[30:31]
	s_cmp_lg_u32 s17, 0
	s_cbranch_scc1 .Lg_nofix
	v_cmp_gt_u32_e32 vcc, 16, v1
	s_and_saveexec_b64 s[30:31], vcc
	v_lshl_add_u32 v228, v1, 2, v196
	ds_read_b32 v229, v228
	ds_read_b32 v230, v228 offset:1024
	s_waitcnt lgkmcnt(0)
	v_add_u32_e32 v229, v229, v230
	ds_write_b32 v228, v229
	s_mov_b64 exec, s[30:31]
